# stack11 + attention unit boundaries no longer drain the four output stores just issued (counted waits: vmcnt(4), explicit vmcnt(0) only on the not-prefetched path)
# baseline (speedup 1.0000x reference)
; #define ATT_BAR() do { asm volatile("s_waitcnt lgkmcnt(0)" ::: "memory"); __builtin_amdgcn_s_barrier(); asm volatile("" ::: "memory"); } while (0)
; __device__ __forceinline__ void unit_diff(const P& p, LAS unsigned char* lds, const Src& S, float lam, bf16_t* orow, const int wid,
;                                           bf16x8 (&qr)[4], const bool pre  , const bool pn  , const Src& Sn) {
;     ...
;     if (pn) {
; #pragma unroll
;         for (int d0 = 0; d0 < 4; ++d0) qr[d0] = qn[d0]; }
; __device__ __forceinline__ void phase(const P& p, LAS unsigned char* lds, int G, int vcu, const int wid) {
;     ...
;     for (int U = vcu; U < NB * 8 * 16; U += G) {
;         if (iter++ == cslot) { ATT_BAR(); f8_share(p, lds, G, vcu, wid); ATT_BAR(); }
;         ATT_DIFF_SRC(U, S, h, tok0, b);
;         const int Un = U + G; const bool pn = Un < NB * 8 * 16 && iter != cslot;
;         ATT_DIFF_SRC(pn ? Un : U, Sn, hn, tok0n, bn);
;         unit_diff(p, lds, S, lam, MX + ((size_t)b * SEQ + tok0) * DM + 512 + h * 64, wid, qrd, pred, pn, Sn);
;         pred = pn;
;     }
.LBB7_397:
	s_waitcnt vmcnt(4)
	v_mov_b32_e32 v178, v92
	v_mov_b32_e32 v177, v93
	v_mov_b32_e32 v176, v94
	v_mov_b32_e32 v175, v95
	v_mov_b32_e32 v174, v88
	v_mov_b32_e32 v173, v89
	v_mov_b32_e32 v172, v90
	v_mov_b32_e32 v161, v91
	v_mov_b32_e32 v160, v76
	v_mov_b32_e32 v155, v77
	v_mov_b32_e32 v154, v78
	v_mov_b32_e32 v153, v79
	v_mov_b32_e32 v152, v72
	v_mov_b32_e32 v151, v73
	v_mov_b32_e32 v150, v74
	v_mov_b32_e32 v145, v75
	s_and_b64 vcc, exec, s[0:1]
	s_cbranch_vccnz .LBB7_446

; #define LAS __attribute__((address_space(3)))
; __device__ __forceinline__ int fresh_lane() { unsigned z = 0u; asm volatile("" : "+v"(z)); return (int)__builtin_amdgcn_mbcnt_hi(~0u, __builtin_amdgcn_mbcnt_lo(~0u, z)); }
; #define ATT_BAR() do { asm volatile("s_waitcnt lgkmcnt(0)" ::: "memory"); __builtin_amdgcn_s_barrier(); asm volatile("" ::: "memory"); } while (0)
; #define ATT_DMA(j, slot) ATT_DMA_S(S, j, slot)
; #define ATT_DMA(j, slot) ATT_DMA_S(S, j, slot)
; #define ATT_DMA(j, slot) ATT_DMA_S(S, j, slot)
; __device__ __forceinline__ void unit_diff(const P& p, LAS unsigned char* lds, const Src& S, float lam, bf16_t* orow, const int wid,
;                                           bf16x8 (&qr)[4], const bool pre  , const bool pn  , const Src& Sn) {
;     const int lane = fresh_lane(), tid = wid * 64 + lane, r32 = lane & 31, hi = lane >> 5;
;     constexpr int NTR = 64;
;     ...
;     if (!pre) {
; #pragma unroll
;         for (int d0 = 0; d0 < 4; ++d0) qr[d0] = *(const bf16x8*)(S.q + (size_t)r32 * 64 + d0 * 16 + hi * 8);
;         ATT_DMA(0, 0); ATT_DMA(1, SLOTB); }
; __device__ __forceinline__ void phase(const P& p, LAS unsigned char* lds, int G, int vcu, const int wid) {
;     ...
;     for (int U = vcu; U < NB * 8 * 16; U += G) {
;         if (iter++ == cslot) { ATT_BAR(); f8_share(p, lds, G, vcu, wid); ATT_BAR(); }
;         ATT_DIFF_SRC(U, S, h, tok0, b);
;         const int Un = U + G; const bool pn = Un < NB * 8 * 16 && iter != cslot;
;         ATT_DIFF_SRC(pn ? Un : U, Sn, hn, tok0n, bn);
;         unit_diff(p, lds, S, lam, MX + ((size_t)b * SEQ + tok0) * DM + 512 + h * 64, wid, qrd, pred, pn, Sn);
.LBB7_433:
	s_ashr_i32 s58, s95, 4
	s_lshl_b32 s2, s95, 8
	s_and_b32 s2, s2, 0xf00
	s_ashr_i32 s59, s58, 31
	s_waitcnt vmcnt(4)
	v_mov_b32_e32 v0, v157
	s_xor_b64 s[0:1], s[54:55], -1
	s_add_i32 s8, s2, s90
	s_lshl_b64 s[60:61], s[58:59], 19
	s_add_u32 s56, s6, s60
	v_mbcnt_lo_u32_b32 v0, -1, v0
	s_addc_u32 s57, s7, s61
	v_mbcnt_hi_u32_b32 v169, -1, v0
	v_readlane_b32 s2, v254, 5
	s_add_u32 s54, s92, s60
	v_ashrrev_i32_e32 v170, 5, v169
	v_add_u32_e32 v0, s2, v169
	s_addc_u32 s55, s4, s61
	v_and_b32_e32 v171, 31, v169
	s_and_b64 vcc, exec, s[0:1]
	v_readfirstlane_b32 s0, v0
	v_lshlrev_b32_e32 v158, 3, v170
	v_lshlrev_b32_e32 v0, 3, v0
	v_readfirstlane_b32 s1, v1
	v_lshlrev_b32_e32 v156, 7, v171
	v_ashrrev_i32_e32 v159, 31, v158
	v_ashrrev_i32_e32 v1, 31, v0
	s_cbranch_vccz .LBB7_435
	s_lshl_b64 s[0:1], s[58:59], 19
	s_add_u32 s2, s34, s0
	s_addc_u32 s13, s35, s1
	s_lshl_b64 s[10:11], s[8:9], 7
	s_add_u32 s10, s2, s10
	s_addc_u32 s11, s13, s11
	v_lshl_add_u64 v[2:3], s[10:11], 0, v[156:157]
	v_lshl_add_u64 v[2:3], v[158:159], 1, v[2:3]
	global_load_dwordx4 v[128:131], v[2:3], off
	global_load_dwordx4 v[132:135], v[2:3], off offset:32
	global_load_dwordx4 v[136:139], v[2:3], off offset:64
	global_load_dwordx4 v[140:143], v[2:3], off offset:96
	v_lshlrev_b64 v[2:3], 1, v[0:1]
	s_mov_b32 m0, s91
	s_waitcnt vmcnt(18)
	v_lshl_add_u64 v[4:5], s[56:57], 0, v[2:3]
	global_load_lds_dwordx4 v[4:5], off
	v_lshl_add_u64 v[2:3], s[54:55], 0, v[2:3]
	s_mov_b32 m0, s15
	v_lshl_add_u64 v[4:5], v[4:5], 0, s[46:47]
	global_load_lds_dwordx4 v[2:3], off
	s_add_i32 m0, s91, 0x4000
	v_lshl_add_u64 v[2:3], v[2:3], 0, s[46:47]
	global_load_lds_dwordx4 v[4:5], off
	s_add_i32 m0, s91, 0x6000
	s_nop 0
	global_load_lds_dwordx4 v[2:3], off
	s_waitcnt vmcnt(0)
	s_cbranch_execz .LBB7_436
	s_branch .LBB7_437
.LBB7_435:
.LBB7_436:
	s_mov_b64 s[0:1], s[60:61]
	s_waitcnt vmcnt(4)
	v_mov_b32_e32 v128, v178
	v_mov_b32_e32 v129, v177
	v_mov_b32_e32 v130, v176
	v_mov_b32_e32 v131, v175
	v_mov_b32_e32 v132, v174
	v_mov_b32_e32 v133, v173
	v_mov_b32_e32 v134, v172
	v_mov_b32_e32 v135, v161
	v_mov_b32_e32 v136, v160
	v_mov_b32_e32 v137, v155
	v_mov_b32_e32 v138, v154
	v_mov_b32_e32 v139, v153
	v_mov_b32_e32 v140, v152
	v_mov_b32_e32 v141, v151
	v_mov_b32_e32 v142, v150
	v_mov_b32_e32 v143, v145
; #define LAS __attribute__((address_space(3)))
; template <bool HAVE_PREV, bool HAVE_NEXT> __device__ __forceinline__ void dstep(f32x16& ca, f32x16& cb, f32x16& pa, f32x16& pb, const bf16x8 (&kf)[4], bf16x8 (&kn)[4], const LAS unsigned char* kbn, unsigned vpa, ...
;     const f32x16 z = {0.f, 0.f, 0.f, 0.f, 0.f, 0.f, 0.f, 0.f, 0.f, 0.f, 0.f, 0.f, 0.f, 0.f, 0.f, 0.f};
;     s16x4 vl[2][2], vh[2][2]; u32x4 wa[2], wb[2];
;     ca = __builtin_amdgcn_mfma_f32_32x32x16_bf16(kf[0], qr[0], z, 0, 0, 0);
;     float a0, a1, a2, a3, a4, a5, a6, a7, b0, b1, b2, b3, b4, b5, b6, b7;
;     if (HAVE_PREV) { a0 = fadd_s(pa[0], pa[1]); a1 = fadd_s(pa[2], pa[3]); a2 = fadd_s(pa[4], pa[5]); a3 = fadd_s(pa[6], pa[7]); a4 = fadd_s(pa[8], pa[9]); a5 = fadd_s(pa[10], pa[11]); a6 = fadd_s(pa[12], pa[13]); a7 = fadd_s(pa[14], pa[15]);
;         wa[0].x = cvtpk(pa[0], pa[1]); wa[0].y = cvtpk(pa[2], pa[3]); wa[0].z = cvtpk(pa[4], pa[5]); wa[0].w = cvtpk(pa[6], pa[7]); }
;     ATT_SB();
;     ca = __builtin_amdgcn_mfma_f32_32x32x16_bf16(kf[1], qr[1], ca, 0, 0, 0);
;     if (HAVE_PREV) {
;         ATT_TR(vl[0][0], vpa, 0); ATT_TR(vh[0][0], vpa, 512); ATT_TR(vl[1][0], vpa, 4096); ATT_TR(vh[1][0], vpa, 4096 + 512);
;         ATT_TR(vl[0][1], vpa, 1024); ATT_TR(vh[0][1], vpa, 1024 + 512); ATT_TR(vl[1][1], vpa, 4096 + 1024); ATT_TR(vh[1][1], vpa, 4096 + 1024 + 512);
;         a0 = fadd_s(a0, a1); a2 = fadd_s(a2, a3); a4 = fadd_s(a4, a5); a6 = fadd_s(a6, a7);
;         wa[1].x = cvtpk(pa[8], pa[9]); wa[1].y = cvtpk(pa[10], pa[11]); wa[1].z = cvtpk(pa[12], pa[13]); wa[1].w = cvtpk(pa[14], pa[15]);
;         a0 = fadd_s(a0, a2); a4 = fadd_s(a4, a6); }
;     ATT_SB();
; __device__ __forceinline__ void unit_diff(const P& p, LAS unsigned char* lds, const Src& S, float lam, bf16_t* orow, const int wid,
;                                           bf16x8 (&qr)[4], const bool pre  , const bool pn  , const Src& Sn) {
;     ...
;     const unsigned lbase = (unsigned)(__SIZE_TYPE__)lds;
;     f32x16 A0, B0, A1, B1; bf16x8 kA[4], kB[4];
;     ATT_WAITV(0); ATT_BAR(); ATT_DMA(2, 2 * SLOTB); ATT_DMA(3, 3 * SLOTB);
; #pragma unroll
;     for (int d0 = 0; d0 < 4; ++d0) kA[d0] = *(const LAS bf16x8*)(lds + koff + d0 * 2048);
;     dstep<false, true>(A0, B0, A1, B1, kA, kB, lds + koff + 512, 0u, qr, o1, o2, l1, l2);
;     dstep<true, true>(A1, B1, A0, B0, kB, kA, lds + SLOTB + koff, lbase + voff, qr, o1, o2, l1, l2);
.LBB7_437:
	s_and_b32 s2, s58, 7
	s_lshl_b32 s10, s2, 13
	s_add_u32 s13, s79, s10
	s_addc_u32 s36, s80, 0
	s_add_u32 s10, s13, 0x8000
	s_addc_u32 s11, s36, 0
	v_lshlrev_b64 v[160:161], 1, v[0:1]
	s_add_u32 s13, s13, 0x18000
	s_waitcnt vmcnt(4)
	v_lshl_add_u64 v[0:1], s[56:57], 0, v[160:161]
	s_addc_u32 s36, s36, 0
	s_waitcnt lgkmcnt(0)
	s_barrier
	v_lshl_add_u64 v[2:3], v[0:1], 0, s[48:49]
	s_add_i32 m0, s96, 0x8000
	v_lshl_add_u64 v[0:1], v[0:1], 0, s[50:51]
	global_load_lds_dwordx4 v[2:3], off
	v_lshl_add_u64 v[2:3], s[54:55], 0, v[160:161]
	s_waitcnt vmcnt(5)
	v_lshl_add_u64 v[4:5], v[2:3], 0, s[48:49]
	s_mov_b32 m0, s42
	v_lshlrev_b32_e32 v49, 8, v170
	global_load_lds_dwordx4 v[4:5], off
	s_add_i32 m0, s96, 0xc000
	v_lshlrev_b32_e32 v4, 4, v169
	global_load_lds_dwordx4 v[0:1], off
	v_lshl_add_u64 v[0:1], v[2:3], 0, s[50:51]
	s_mov_b32 m0, s43
	v_lshlrev_b32_e32 v2, 3, v169
	global_load_lds_dwordx4 v[0:1], off
	v_lshlrev_b32_e32 v0, 4, v171
	v_lshl_or_b32 v0, v170, 10, v0
	v_lshlrev_b32_e32 v1, 1, v169
	v_and_b32_e32 v1, 32, v1
	v_add_u32_e32 v173, 0, v0
	v_and_or_b32 v48, v2, 24, v1
	ds_read_b128 v[0:3], v173
	s_waitcnt lgkmcnt(0)
	v_mfma_f32_32x32x16_bf16 v[16:31], v[0:3], v[128:131], 0
	v_and_b32_e32 v50, 0xc0, v4
	ds_read_b128 v[4:7], v173 offset:2048
	ds_read_b128 v[8:11], v173 offset:4096
	ds_read_b128 v[32:35], v173 offset:6144
	s_mov_b32 s59, 0x8000
	s_mov_b32 s37, 0xc000
	s_waitcnt lgkmcnt(0)
	v_mfma_f32_32x32x16_bf16 v[16:31], v[4:7], v[132:135], v[16:31]
	v_mfma_f32_32x32x16_bf16 v[0:15], v[8:11], v[136:139], 0
	v_mfma_f32_32x32x16_bf16 v[0:15], v[32:35], v[140:143], v[0:15]
	s_waitcnt lgkmcnt(0)
	ds_read_b128 v[36:39], v173 offset:512
	ds_read_b128 v[40:43], v173 offset:2560
	ds_read_b128 v[44:47], v173 offset:4608
	ds_read_b128 v[32:35], v173 offset:6656
	s_nop 5
	v_exp_f32_e32 v16, v16
	v_exp_f32_e32 v17, v17
	v_exp_f32_e32 v18, v18
	v_exp_f32_e32 v19, v19
	s_nop 0
	v_exp_f32_e32 v20, v20
	v_exp_f32_e32 v21, v21
	v_exp_f32_e32 v22, v22
	v_exp_f32_e32 v23, v23
	s_nop 0
	v_exp_f32_e32 v24, v24
	v_exp_f32_e32 v25, v25
	v_exp_f32_e32 v26, v26
	v_exp_f32_e32 v27, v27
	s_nop 0
	v_exp_f32_e32 v28, v28
	v_exp_f32_e32 v29, v29
	v_exp_f32_e32 v30, v30
	v_exp_f32_e32 v31, v31
	v_exp_f32_e32 v0, v0
	v_exp_f32_e32 v1, v1
	v_exp_f32_e32 v2, v2
	v_exp_f32_e32 v3, v3
	s_nop 0
	v_exp_f32_e32 v4, v4
	v_exp_f32_e32 v5, v5
	v_exp_f32_e32 v6, v6
	v_exp_f32_e32 v7, v7
	s_nop 0
	v_exp_f32_e32 v8, v8
	v_exp_f32_e32 v9, v9
	v_exp_f32_e32 v10, v10
	v_exp_f32_e32 v11, v11
	s_nop 0
	v_exp_f32_e32 v12, v12
	v_exp_f32_e32 v13, v13
	v_exp_f32_e32 v14, v14
	v_exp_f32_e32 v15, v15
	s_waitcnt lgkmcnt(0)
	v_mfma_f32_32x32x16_bf16 v[80:95], v[36:39], v[128:131], 0
	s_add_i32 s53, 0, 0x2000
	v_add_u32_e32 v50, s53, v50
	v_add3_u32 v172, v50, v49, v48
	v_add_f32_e32 v52, v16, v17
	v_add_f32_e32 v53, v18, v19
	v_add_f32_e32 v54, v20, v21
	v_add_f32_e32 v55, v22, v23
	v_add_f32_e32 v56, v24, v25
	v_add_f32_e32 v57, v26, v27
	v_add_f32_e32 v58, v28, v29
	v_add_f32_e32 v59, v30, v31
	v_cvt_pk_bf16_f32 v16, v16, v17
	v_cvt_pk_bf16_f32 v17, v18, v19
	v_cvt_pk_bf16_f32 v18, v20, v21
	v_cvt_pk_bf16_f32 v19, v22, v23
	ds_read_b64_tr_b16 v[36:37], v172 offset:0
	ds_read_b64_tr_b16 v[38:39], v172 offset:512
	ds_read_b64_tr_b16 v[48:49], v172 offset:4096
	v_mfma_f32_32x32x16_bf16 v[80:95], v[40:43], v[132:135], v[80:95]
	ds_read_b64_tr_b16 v[50:51], v172 offset:4608
	ds_read_b64_tr_b16 v[104:105], v172 offset:1024
	ds_read_b64_tr_b16 v[106:107], v172 offset:1536
	ds_read_b64_tr_b16 v[100:101], v172 offset:5120
	ds_read_b64_tr_b16 v[102:103], v172 offset:5632
	v_add_f32_e32 v20, v52, v53
	v_add_f32_e32 v21, v54, v55
	v_add_f32_e32 v22, v56, v57
	v_add_f32_e32 v23, v58, v59
	v_cvt_pk_bf16_f32 v108, v24, v25
	v_cvt_pk_bf16_f32 v109, v26, v27
	v_cvt_pk_bf16_f32 v110, v28, v29
	v_cvt_pk_bf16_f32 v111, v30, v31
	s_nop 0
	v_add_f32_e32 v20, v20, v21
	v_add_f32_e32 v21, v22, v23
	v_mfma_f32_32x32x16_bf16 v[64:79], v[44:47], v[136:139], 0
	v_add_f32_e32 v22, v0, v1
	v_add_f32_e32 v23, v2, v3
	v_add_f32_e32 v24, v4, v5
	v_add_f32_e32 v25, v6, v7
	v_add_f32_e32 v26, v8, v9
	v_add_f32_e32 v27, v10, v11
	v_add_f32_e32 v28, v12, v13
	v_add_f32_e32 v29, v14, v15
	v_cvt_pk_bf16_f32 v52, v0, v1
	v_cvt_pk_bf16_f32 v53, v2, v3
	v_cvt_pk_bf16_f32 v54, v4, v5
	v_cvt_pk_bf16_f32 v55, v6, v7
	v_add_f32_e32 v0, v20, v21
	v_mfma_f32_32x32x16_bf16 v[64:79], v[32:35], v[140:143], v[64:79]
	v_add_f32_e32 v1, v22, v23
	v_add_f32_e32 v2, v24, v25
	v_add_f32_e32 v3, v26, v27
	v_add_f32_e32 v4, v28, v29
	v_cvt_pk_bf16_f32 v112, v8, v9
	v_cvt_pk_bf16_f32 v113, v10, v11
	v_cvt_pk_bf16_f32 v114, v12, v13
	v_cvt_pk_bf16_f32 v115, v14, v15
	s_nop 0
	v_add_f32_e32 v1, v1, v2
	v_add_f32_e32 v2, v3, v4
	v_add_f32_e32 v174, v166, v0
	s_mov_b32 s60, 0
	v_add_f32_e32 v0, v1, v2
	s_waitcnt lgkmcnt(0)
	s_nop 0
	v_add_f32_e32 v175, v166, v0
	v_mfma_f32_32x32x16_bf16 v[0:15], v[16:19], v[36:39], 0
	ds_read_b128 v[96:99], v173 offset:16384
	ds_read_b128 v[152:155], v173 offset:18432
	ds_read_b128 v[148:151], v173 offset:20480
	ds_read_b128 v[144:147], v173 offset:22528
	s_nop 0
	v_exp_f32_e32 v80, v80
	v_exp_f32_e32 v81, v81
	v_exp_f32_e32 v82, v82
	v_exp_f32_e32 v83, v83
	v_mfma_f32_32x32x16_bf16 v[16:31], v[16:19], v[48:51], 0
	v_exp_f32_e32 v84, v84
	v_exp_f32_e32 v85, v85
	v_exp_f32_e32 v86, v86
	v_exp_f32_e32 v87, v87
	v_mfma_f32_32x32x16_bf16 v[32:47], v[52:55], v[36:39], 0
	v_exp_f32_e32 v88, v88
	v_exp_f32_e32 v89, v89
	v_exp_f32_e32 v90, v90
	v_exp_f32_e32 v91, v91
	v_mfma_f32_32x32x16_bf16 v[48:63], v[52:55], v[48:51], 0
	v_exp_f32_e32 v92, v92
	v_exp_f32_e32 v93, v93
	v_exp_f32_e32 v94, v94
	v_exp_f32_e32 v95, v95
	v_mfma_f32_32x32x16_bf16 v[0:15], v[108:111], v[104:107], v[0:15]
	v_exp_f32_e32 v64, v64
	v_exp_f32_e32 v65, v65
	v_exp_f32_e32 v66, v66
	v_exp_f32_e32 v67, v67
	v_mfma_f32_32x32x16_bf16 v[16:31], v[108:111], v[100:103], v[16:31]
	v_exp_f32_e32 v68, v68
	v_exp_f32_e32 v69, v69
	v_exp_f32_e32 v70, v70
	v_exp_f32_e32 v71, v71
	v_mfma_f32_32x32x16_bf16 v[32:47], v[112:115], v[104:107], v[32:47]
	v_exp_f32_e32 v72, v72
	v_exp_f32_e32 v73, v73
	v_exp_f32_e32 v74, v74
	v_exp_f32_e32 v75, v75
	v_mfma_f32_32x32x16_bf16 v[48:63], v[112:115], v[100:103], v[48:63]
	v_exp_f32_e32 v76, v76
	v_exp_f32_e32 v77, v77
	v_exp_f32_e32 v78, v78
	v_exp_f32_e32 v79, v79
	s_add_u32 s54, s30, s0
	v_add_u32_e32 v176, 0x800, v172
	s_addc_u32 s55, s31, s1
	s_mov_b32 s57, 0x10000
	s_movk_i32 s56, 0x4000
	s_mov_b64 s[0:1], 0

; #define ATT_BAR() do { asm volatile("s_waitcnt lgkmcnt(0)" ::: "memory"); __builtin_amdgcn_s_barrier(); asm volatile("" ::: "memory"); } while (0)
; __device__ __forceinline__ void unit_swa(const P& p, LAS unsigned char* lds, const Src& S, const int qa  , const float sinkp, bf16_t* orow, const int wid,
;                                          bf16x8 (&qr)[4], const bool pre, const bool pn, const Src& Sn) {
;     ...
;     if (pn) {
; #pragma unroll
;         for (int d0 = 0; d0 < 4; ++d0) qr[d0] = qn[d0]; }
;     else ATT_BAR();
; __device__ __forceinline__ void phase(const P& p, LAS unsigned char* lds, int G, int vcu, const int wid) {
;     ...
;     for (int U = vcu; U < NB * 2 * 32 * 2; U += G) {
;         if (iter++ == cslot) { ATT_BAR(); f8_share(p, lds, G, vcu, wid); ATT_BAR(); }
;         ATT_SWA_SRC(U, S, hq, tok0, b);
;         const int Un = U + G; const bool pn = Un < NB * 2 * 32 * 2 && iter != cslot;
;         ATT_SWA_SRC(pn ? Un : U, Sn, hqn, tok0n, bn);
;         unit_swa(p, lds, S, tok0, exp2f(p.sink[hq] * LOG2E), MX + ((size_t)b * SEQ + tok0) * DM + hq * 64, wid, qra, pre, pn, Sn);
;         pre = pn;
.LBB7_450:
	s_waitcnt vmcnt(4)
	v_mov_b32_e32 v157, v44
	v_mov_b32_e32 v172, v45
	v_mov_b32_e32 v171, v46
	v_mov_b32_e32 v170, v47
	v_mov_b32_e32 v169, v40
	v_mov_b32_e32 v168, v41
	v_mov_b32_e32 v167, v42
	v_mov_b32_e32 v166, v43
	v_mov_b32_e32 v165, v36
	v_mov_b32_e32 v164, v37
	v_mov_b32_e32 v163, v38
	v_mov_b32_e32 v162, v39
	v_mov_b32_e32 v161, v32
	v_mov_b32_e32 v160, v33
	v_mov_b32_e32 v159, v34
	v_mov_b32_e32 v158, v35
	s_and_b64 vcc, exec, s[46:47]
	s_cbranch_vccnz .LBB7_515

; #define LAS __attribute__((address_space(3)))
; __device__ __forceinline__ int fresh_lane() { unsigned z = 0u; asm volatile("" : "+v"(z)); return (int)__builtin_amdgcn_mbcnt_hi(~0u, __builtin_amdgcn_mbcnt_lo(~0u, z)); }
; #define ATT_BAR() do { asm volatile("s_waitcnt lgkmcnt(0)" ::: "memory"); __builtin_amdgcn_s_barrier(); asm volatile("" ::: "memory"); } while (0)
; #define ATT_DMA(j, slot) ATT_DMA_S(S, j, slot)
; #define ATT_DMA(j, slot) ATT_DMA_S(S, j, slot)
; #define ATT_DMA(j, slot) ATT_DMA_S(S, j, slot)
; __device__ __forceinline__ void unit_swa(const P& p, LAS unsigned char* lds, const Src& S, const int qa  , const float sinkp, bf16_t* orow, const int wid,
;                                          bf16x8 (&qr)[4], const bool pre, const bool pn, const Src& Sn) {
;     const int lane = fresh_lane(), tid = wid * 64 + lane, r32 = lane & 31, hi = lane >> 5;
;     const int NTR = S.ntr;
;     ...
;     if (!pre) {
; #pragma unroll
;         for (int d0 = 0; d0 < 4; ++d0) qr[d0] = *(const bf16x8*)(S.q + (size_t)r32 * 64 + d0 * 16 + hi * 8);
;         ATT_DMA(0, 0); ATT_DMA(1, SLOTB); }
; __device__ __forceinline__ void phase(const P& p, LAS unsigned char* lds, int G, int vcu, const int wid) {
;     ...
;     for (int U = vcu; U < NB * 2 * 32 * 2; U += G) {
;         if (iter++ == cslot) { ATT_BAR(); f8_share(p, lds, G, vcu, wid); ATT_BAR(); }
;         ATT_SWA_SRC(U, S, hq, tok0, b);
;         const int Un = U + G; const bool pn = Un < NB * 2 * 32 * 2 && iter != cslot;
;         ATT_SWA_SRC(pn ? Un : U, Sn, hqn, tok0n, bn);
;         unit_swa(p, lds, S, tok0, exp2f(p.sink[hq] * LOG2E), MX + ((size_t)b * SEQ + tok0) * DM + hq * 64, wid, qra, pre, pn, Sn);
.LBB7_485:
	s_ashr_i32 s36, s41, 6
	s_lshl_b32 s9, s41, 1
	s_and_b32 s6, s36, 1
	s_and_b32 s9, s9, 2
	s_bfe_u32 s1, s41, 0x50001
	s_lshl_b32 s8, s6, 2
	s_add_i32 s9, s9, s33
	s_add_i32 s8, s9, s8
	s_lshl_b32 s9, s1, 7
	s_lshl_b32 s11, s1, 1
	s_xor_b64 s[56:57], s[44:45], -1
	s_ashr_i32 s0, s41, 7
	s_or_b32 s9, s9, s34
	s_add_i32 s37, s11, -2
	s_cmp_lg_u32 s1, 0
	s_cselect_b32 s44, s37, 0
	s_add_i32 s11, s11, 3
	s_cmp_lg_u32 s1, 31
	s_cselect_b32 s54, s11, 63
	s_ashr_i32 s37, s36, 31
	s_lshl_b64 s[36:37], s[36:37], 19
	s_add_u32 s1, s13, s36
	s_addc_u32 s11, s81, s37
	s_add_u32 s36, s82, s36
	s_addc_u32 s37, s84, s37
	s_lshl_b32 s6, s6, 13
	s_add_u32 s38, s79, s6
	s_addc_u32 s48, s80, 0
	s_add_u32 s49, s38, 0x4000
	s_addc_u32 s50, s48, 0
	s_lshl_b32 s6, s8, 2
	v_readlane_b32 s60, v254, 25
	s_waitcnt vmcnt(4)
	v_mov_b32_e32 v0, s6
	v_readlane_b32 s61, v254, 26
	v_readlane_b32 s6, v254, 5
	s_sub_i32 s51, s54, s44
	s_mov_b64 s[46:47], -1
	s_and_b64 vcc, exec, s[56:57]
	v_readlane_b32 s62, v254, 27
	s_cbranch_vccz .Lswa_sink_keep
	global_load_dword v111, v0, s[60:61]
.Lswa_sink_keep:
	v_mov_b32_e32 v0, v145
	v_readlane_b32 s63, v254, 28
	v_mbcnt_lo_u32_b32 v0, -1, v0
	v_mbcnt_hi_u32_b32 v108, -1, v0
	v_add_u32_e32 v0, s6, v108
	v_ashrrev_i32_e32 v109, 5, v108
	v_and_b32_e32 v110, 31, v108
	v_lshlrev_b32_e32 v104, 3, v109
	v_lshlrev_b32_e32 v0, 3, v0
	v_lshlrev_b32_e32 v144, 7, v110
	v_ashrrev_i32_e32 v105, 31, v104
	v_ashrrev_i32_e32 v1, 31, v0
	v_readlane_b32 s64, v254, 29
	v_readlane_b32 s65, v254, 30
	v_readlane_b32 s66, v254, 31
	v_readlane_b32 s67, v254, 32
	v_readlane_b32 s68, v254, 33
	v_readlane_b32 s69, v254, 34
	v_readlane_b32 s70, v254, 35
	v_readlane_b32 s71, v254, 36
	v_readlane_b32 s72, v254, 37
	v_readlane_b32 s73, v254, 38
	v_readlane_b32 s74, v254, 39
	v_readlane_b32 s75, v254, 40
	s_cbranch_vccz .LBB7_487
	s_lshl_b32 s6, s0, 3
	s_add_i32 s46, s8, s6
	s_ashr_i32 s47, s46, 31
	s_lshl_b64 s[46:47], s[46:47], 19
	s_add_u32 s6, s5, s46
	s_addc_u32 s45, s12, s47
	s_lshl_b32 s46, s9, 7
	s_add_u32 s46, s6, s46
	s_addc_u32 s47, s45, 0
	s_ashr_i32 s45, s44, 31
	v_lshl_add_u64 v[2:3], s[46:47], 0, v[144:145]
	s_lshl_b64 s[46:47], s[44:45], 13
	s_add_u32 s6, s1, s46
	s_addc_u32 s45, s11, s47
	s_add_u32 s55, s36, s46
	s_addc_u32 s56, s37, s47
	v_lshl_add_u64 v[2:3], v[104:105], 1, v[2:3]
	s_cmp_gt_i32 s51, -1
	global_load_dwordx4 v[64:67], v[2:3], off
	global_load_dwordx4 v[68:71], v[2:3], off offset:32
	global_load_dwordx4 v[72:75], v[2:3], off offset:64
	global_load_dwordx4 v[76:79], v[2:3], off offset:96
	s_cselect_b32 s47, s45, s48
	s_cselect_b32 s46, s6, s38
	v_lshlrev_b64 v[2:3], 1, v[0:1]
	s_cselect_b32 s57, s56, s50
	s_cselect_b32 s56, s55, s49
	s_waitcnt lgkmcnt(0)
	v_lshl_add_u64 v[4:5], s[46:47], 0, v[2:3]
	s_or_b32 s46, s44, 1
	s_ashr_i32 s47, s46, 31
	s_lshl_b64 s[46:47], s[46:47], 13
	s_add_u32 s6, s1, s46
	s_addc_u32 s45, s11, s47
	s_mov_b32 m0, s35
	s_add_u32 s55, s36, s46
	global_load_lds_dwordx4 v[4:5], off
	v_lshl_add_u64 v[4:5], s[56:57], 0, v[2:3]
	s_addc_u32 s56, s37, s47
	s_cmp_gt_i32 s51, 0
	s_mov_b32 m0, s10
	s_cselect_b32 s47, s45, s48
	s_cselect_b32 s46, s6, s38
	global_load_lds_dwordx4 v[4:5], off
	s_cselect_b32 s57, s56, s50
	s_cselect_b32 s56, s55, s49
	v_lshl_add_u64 v[4:5], s[46:47], 0, v[2:3]
	s_add_i32 m0, s35, 0x4000
	v_lshl_add_u64 v[2:3], s[56:57], 0, v[2:3]
	global_load_lds_dwordx4 v[4:5], off
	s_add_i32 m0, s35, 0x6000
	s_mov_b64 s[46:47], 0
	global_load_lds_dwordx4 v[2:3], off
	s_waitcnt vmcnt(0)
.LBB7_487:
	s_andn2_b64 vcc, exec, s[46:47]
	s_cbranch_vccnz .LBB7_489
	s_waitcnt vmcnt(4)
	v_mov_b32_e32 v64, v157
	v_mov_b32_e32 v65, v172
	v_mov_b32_e32 v66, v171
	v_mov_b32_e32 v67, v170
	v_mov_b32_e32 v68, v169
	v_mov_b32_e32 v69, v168
	v_mov_b32_e32 v70, v167
	v_mov_b32_e32 v71, v166
	v_mov_b32_e32 v72, v165
	v_mov_b32_e32 v73, v164
	v_mov_b32_e32 v74, v163
	v_mov_b32_e32 v75, v162
	v_mov_b32_e32 v76, v161
	v_mov_b32_e32 v77, v160
	v_mov_b32_e32 v78, v159
	v_mov_b32_e32 v79, v158
; #define LAS __attribute__((address_space(3)))
; template <bool HAVE_PREV, bool HAVE_NEXT> __device__ __forceinline__ void sstep(f32x16& ca, f32x16& pa, const bf16x8 (&kf)[4], bf16x8 (&kn)[4], const LAS unsigned char* kbn, unsigned vpa, ...
;     const f32x16 z = {0.f, 0.f, 0.f, 0.f, 0.f, 0.f, 0.f, 0.f, 0.f, 0.f, 0.f, 0.f, 0.f, 0.f, 0.f, 0.f};
;     s16x4 vl[2][2], vh[2][2]; u32x4 wa[2];
;     ca = __builtin_amdgcn_mfma_f32_32x32x16_bf16(kf[0], qr[0], z, 0, 0, 0);
;     float a0, a1, a2, a3, a4, a5, a6, a7;
;     if (HAVE_PREV) { a0 = fadd_s(pa[0], pa[1]); a1 = fadd_s(pa[2], pa[3]); a2 = fadd_s(pa[4], pa[5]); a3 = fadd_s(pa[6], pa[7]); a4 = fadd_s(pa[8], pa[9]); a5 = fadd_s(pa[10], pa[11]); a6 = fadd_s(pa[12], pa[13]); a7 = fadd_s(pa[14], pa[15]);
;         wa[0].x = cvtpk(pa[0], pa[1]); wa[0].y = cvtpk(pa[2], pa[3]); wa[0].z = cvtpk(pa[4], pa[5]); wa[0].w = cvtpk(pa[6], pa[7]); }
;     ATT_SB();
;     ca = __builtin_amdgcn_mfma_f32_32x32x16_bf16(kf[1], qr[1], ca, 0, 0, 0);
;     if (HAVE_PREV) {
;         ATT_TR(vl[0][0], vpa, 0); ATT_TR(vh[0][0], vpa, 512); ATT_TR(vl[1][0], vpa, 4096); ATT_TR(vh[1][0], vpa, 4096 + 512);
;         ATT_TR(vl[0][1], vpa, 1024); ATT_TR(vh[0][1], vpa, 1024 + 512); ATT_TR(vl[1][1], vpa, 4096 + 1024); ATT_TR(vh[1][1], vpa, 4096 + 1024 + 512);
;         a0 = fadd_s(a0, a1); a2 = fadd_s(a2, a3); a4 = fadd_s(a4, a5); a6 = fadd_s(a6, a7);
;         wa[1].x = cvtpk(pa[8], pa[9]); wa[1].y = cvtpk(pa[10], pa[11]); wa[1].z = cvtpk(pa[12], pa[13]); wa[1].w = cvtpk(pa[14], pa[15]); }
;     ATT_SB();
;     ca = __builtin_amdgcn_mfma_f32_32x32x16_bf16(kf[2], qr[2], ca, 0, 0, 0);
;     if (HAVE_PREV) { a0 = fadd_s(a0, a2); a4 = fadd_s(a4, a6); }
;     ATT_SB();
; __device__ __forceinline__ void unit_swa(const P& p, LAS unsigned char* lds, const Src& S, const int qa  , const float sinkp, bf16_t* orow, const int wid,
;                                          bf16x8 (&qr)[4], const bool pre, const bool pn, const Src& Sn) {
;     ...
;     ATT_WAITV(0); ATT_BAR(); ATT_DMA(2, 2 * SLOTB); ATT_DMA(3, 3 * SLOTB);
; #pragma unroll
;     for (int d0 = 0; d0 < 4; ++d0) kA[d0] = *(const LAS bf16x8*)(lds + koff + d0 * 2048);
;     sstep<false, true>(A0, A1, kA, kB, lds + koff + 512, 0u, qr, o1, l1, SW_FULL(0, 0), SW_DQ(0, 0));
;     sstep<true, true>(A1, A0, kB, kA, lds + SLOTB + koff, lbase + voff, qr, o1, l1, SW_FULL(0, 1), SW_DQ(0, 1));
.LBB7_489:
	s_add_i32 s6, s44, 2
	s_lshl_b32 s58, s44, 6
	s_lshl_b64 s[46:47], s[6:7], 13
	s_add_u32 s6, s1, s46
	s_addc_u32 s45, s11, s47
	s_add_u32 s55, s36, s46
	s_addc_u32 s56, s37, s47
	s_cmp_gt_i32 s51, 1
	s_cselect_b32 s47, s45, s48
	s_cselect_b32 s46, s6, s38
	s_cselect_b32 s57, s56, s50
	s_cselect_b32 s56, s55, s49
	v_lshlrev_b64 v[106:107], 1, v[0:1]
	s_add_i32 s6, s44, 3
	v_lshl_add_u64 v[0:1], s[46:47], 0, v[106:107]
	s_lshl_b64 s[46:47], s[6:7], 13
	s_add_u32 s6, s1, s46
	s_waitcnt vmcnt(4)
	s_addc_u32 s45, s11, s47
	s_mov_b32 m0, s85
	s_waitcnt lgkmcnt(0)
	s_barrier
	s_add_u32 s55, s36, s46
	global_load_lds_dwordx4 v[0:1], off
	v_lshl_add_u64 v[0:1], s[56:57], 0, v[106:107]
	s_addc_u32 s56, s37, s47
	s_cmp_gt_i32 s51, 2
	s_mov_b32 m0, s87
	s_cselect_b32 s47, s45, s48
	s_cselect_b32 s46, s6, s38
	global_load_lds_dwordx4 v[0:1], off
	s_cselect_b32 s57, s56, s50
	s_cselect_b32 s56, s55, s49
	v_lshl_add_u64 v[0:1], s[46:47], 0, v[106:107]
	s_mov_b32 m0, s88
	s_or_b32 s45, s9, 31
	global_load_lds_dwordx4 v[0:1], off
	v_lshl_add_u64 v[0:1], s[56:57], 0, v[106:107]
	s_mov_b32 m0, s90
	s_sub_i32 s6, s58, s9
	global_load_lds_dwordx4 v[0:1], off
	v_lshlrev_b32_e32 v0, 4, v110
	v_lshl_or_b32 v0, v109, 10, v0
	v_add_u32_e32 v114, 0, v0
	ds_read_b128 v[0:3], v114
	ds_read_b128 v[16:19], v114 offset:2048
	ds_read_b128 v[20:23], v114 offset:4096
	ds_read_b128 v[24:27], v114 offset:6144
	s_waitcnt vmcnt(8) lgkmcnt(0)
	v_mfma_f32_32x32x16_bf16 v[0:15], v[0:3], v[64:67], 0
	s_sub_i32 s46, s45, s58
	s_or_b32 s47, s6, 31
	v_lshlrev_b32_e32 v112, 2, v109
	s_max_i32 s46, s46, s47
	v_or_b32_e32 v96, s9, v110
	s_cmpk_lt_i32 s46, 0x81
	v_mfma_f32_32x32x16_bf16 v[0:15], v[16:19], v[68:71], v[0:15]
	v_mfma_f32_32x32x16_bf16 v[0:15], v[20:23], v[72:75], v[0:15]
	v_mfma_f32_32x32x16_bf16 v[0:15], v[24:27], v[76:79], v[0:15]
	s_waitcnt lgkmcnt(0)
	ds_read_b128 v[28:31], v114 offset:512
	ds_read_b128 v[24:27], v114 offset:2560
	ds_read_b128 v[20:23], v114 offset:4608
	ds_read_b128 v[16:19], v114 offset:6656
	s_cbranch_scc1 .LBB7_491
	v_add_u32_e32 v32, s58, v112
	v_sub_u32_e32 v32, v96, v32
	v_add_u32_e32 v33, 0xffffff7f, v32
	v_cmp_lt_u32_e32 vcc, s91, v33
	v_add_u32_e32 v33, 0xffffff7e, v32
	s_nop 1
	v_cndmask_b32_e32 v0, v155, v0, vcc
	v_cmp_lt_u32_e32 vcc, s91, v33
	v_add_u32_e32 v33, 0xffffff7d, v32
	s_nop 0
	v_cndmask_b32_e32 v1, v155, v1, vcc
	v_cmp_lt_u32_e32 vcc, s91, v33
	v_add_u32_e32 v33, 0xffffff7c, v32
	s_nop 0
	v_cndmask_b32_e32 v2, v155, v2, vcc
	v_cmp_lt_u32_e32 vcc, s91, v33
	v_add_u32_e32 v33, 0xffffff77, v32
	s_nop 0
	v_cndmask_b32_e32 v3, v155, v3, vcc
	v_cmp_lt_u32_e32 vcc, s91, v33
	v_add_u32_e32 v33, 0xffffff76, v32
	s_nop 0
	v_cndmask_b32_e32 v4, v155, v4, vcc
	v_cmp_lt_u32_e32 vcc, s91, v33
	v_add_u32_e32 v33, 0xffffff75, v32
	s_nop 0
	v_cndmask_b32_e32 v5, v155, v5, vcc
	v_cmp_lt_u32_e32 vcc, s91, v33
	v_add_u32_e32 v33, 0xffffff74, v32
	s_nop 0
	v_cndmask_b32_e32 v6, v155, v6, vcc
	v_cmp_lt_u32_e32 vcc, s91, v33
	v_add_u32_e32 v33, 0xffffff6f, v32
	s_nop 0
	v_cndmask_b32_e32 v7, v155, v7, vcc
	v_cmp_lt_u32_e32 vcc, s91, v33
	v_add_u32_e32 v33, 0xffffff6e, v32
	s_nop 0
	v_cndmask_b32_e32 v8, v155, v8, vcc
	v_cmp_lt_u32_e32 vcc, s91, v33
	v_add_u32_e32 v33, 0xffffff6d, v32
	s_nop 0
	v_cndmask_b32_e32 v9, v155, v9, vcc
	v_cmp_lt_u32_e32 vcc, s91, v33
	v_add_u32_e32 v33, 0xffffff6c, v32
	s_nop 0
	v_cndmask_b32_e32 v10, v155, v10, vcc
	v_cmp_lt_u32_e32 vcc, s91, v33
	v_add_u32_e32 v33, 0xffffff67, v32
	s_nop 0
	v_cndmask_b32_e32 v11, v155, v11, vcc
	v_cmp_lt_u32_e32 vcc, s91, v33
	v_add_u32_e32 v33, 0xffffff66, v32
	s_nop 0
	v_cndmask_b32_e32 v12, v155, v12, vcc
	v_cmp_lt_u32_e32 vcc, s91, v33
	v_add_u32_e32 v33, 0xffffff65, v32
	v_add_u32_e32 v32, 0xffffff64, v32
	v_cndmask_b32_e32 v13, v155, v13, vcc
	v_cmp_lt_u32_e32 vcc, s91, v33
	s_nop 1
	v_cndmask_b32_e32 v14, v155, v14, vcc
	v_cmp_lt_u32_e32 vcc, s91, v32
	s_nop 1
	v_cndmask_b32_e32 v15, v155, v15, vcc
